# k13: + P9 epilogue VALU trimmed algebraically (exp2-domain glu, (x+1)/c folded, dead clamp removed), peeled C=0 first K iteration
# speedup vs baseline: 1.0297x; 1.0117x over previous
; __device__ __forceinline__ float sigmoidf_(float x) { return __builtin_amdgcn_rcpf(1.0f + __builtin_amdgcn_exp2f(-1.44269504089f * x)); }
; #define PG8_STAGE2(bufoff, gbase, o0, o1) do { \
;         __builtin_amdgcn_global_load_lds((const unsigned*)((const char*)(gbase) + (o0)), (PG8_LAS unsigned*)(lds + (bufoff) + ldsw), 16, 0, 0); \
;         __builtin_amdgcn_global_load_lds((const unsigned*)((const char*)(gbase) + (o1)), (PG8_LAS unsigned*)(lds + (bufoff) + ldsw + 8192), 16, 0, 0); } while (0)
; #define PG8_STAGE_B(bufoff, gbase) PG8_STAGE2(bufoff, gbase, voffB[0], voffB[1])
; #define PG8_WAIT_V(n) asm volatile("s_waitcnt vmcnt(" #n ")" ::: "memory")
; #define PG8_BAR __builtin_amdgcn_s_barrier()
;     ...
;     PG8_STAGE_B(PG8_SB(0, 0), cB + k0); PG8_STAGE_B(PG8_SB(0, 1), cB + hstepB + k0); PG8_STAGE2(PG8_SA(0, 0), cA + k0, gcur[0][0], gcur[0][1]); PG8_STAGE2(PG8_SA(0, 1), cA + hstepA + k0, gcur[1][0], gcur[1][1]);
;     if (wr == 1) PG8_BAR;
;     PG8_WAIT_V(2); PG8_BAR;
;     PG8_STAGE_B(PG8_SB(1, 0), cB + k1); PG8_STAGE2(PG8_SA(1, 0), cA + k1, gcur[0][0], gcur[0][1]); PG8_STAGE_B(PG8_SB(1, 1), cB + hstepB + k1);
;     PG8_WAIT_V(6); PG8_BAR; }
;     __device__ __forceinline__ void operator()(EPI_ARGS) const {
;     ...
;                     const f32x4 a0 = acc[ai][0][m][0] * 0.03125f + ba0, a1 = acc[ai][0][m][1] * 0.03125f + ba1, l0 = acc[ai][1][m][0] * 0.03125f + bl0, l1 = acc[ai][1][m][1] * 0.03125f + bl1;
;                     float o[8];
; #pragma unroll
;                     for (int j = 0; j < 4; ++j) { const float g0 = fminf(a0[j], 7.0f), g1 = fminf(a1[j], 7.0f), x0 = fminf(fmaxf(l0[j], -7.0f), 7.0f), x1 = fminf(fmaxf(l1[j], -7.0f), 7.0f);
;                         o[j] = g0 * sigmoidf_(1.702f * g0) * (x0 + 1.0f); o[4 + j] = g1 * sigmoidf_(1.702f * g1) * (x1 + 1.0f); }
.LBB0_1300:
	s_add_u32 s4, s4, 0x80
	s_addc_u32 s5, s5, 0
	s_cmp_lt_i32 s38, 15
	s_cselect_b32 s18, s5, 0
	s_cselect_b32 s19, s4, 0
	s_lshl_b32 s4, s7, 5
	s_and_b32 s69, s4, 0x60
	s_lshl_b32 s20, s6, 6
	s_lshl_b32 s6, s6, 13
	s_lshl_b32 s7, s69, 7
	s_add_u32 s16, s8, 0x5da00000
	s_addc_u32 s17, s9, 0
	s_add_u32 s4, s36, s19
	s_addc_u32 s5, s37, s18
	s_add_i32 s70, s31, 0x18000
	v_lshl_add_u64 v[4:5], s[4:5], 0, v[196:197]
	s_mov_b32 m0, s70
	s_add_i32 s71, s31, 0x1a000
	s_waitcnt vmcnt(2)
	s_barrier
	global_load_lds_dwordx4 v[4:5], off
	v_lshl_add_u64 v[4:5], s[4:5], 0, v[198:199]
	s_add_u32 s4, s59, s19
	s_mov_b32 m0, s71
	s_addc_u32 s5, s60, s18
	s_add_i32 s72, s31, 0x8000
	global_load_lds_dwordx4 v[4:5], off
	v_lshl_add_u64 v[4:5], s[4:5], 0, v[206:207]
	s_mov_b32 m0, s72
	s_add_i32 s73, s31, 0xa000
	global_load_lds_dwordx4 v[4:5], off
	v_lshl_add_u64 v[4:5], s[4:5], 0, v[204:205]
	s_add_u32 s4, s14, s19
	s_mov_b32 m0, s73
	s_addc_u32 s5, s15, s18
	s_add_i32 s74, s31, 0x1c000
	global_load_lds_dwordx4 v[4:5], off
	v_lshl_add_u64 v[4:5], s[4:5], 0, v[196:197]
	s_mov_b32 m0, s74
	s_add_i32 s75, s31, 0x1e000
	global_load_lds_dwordx4 v[4:5], off
	v_lshl_add_u64 v[4:5], s[4:5], 0, v[198:199]
	s_mov_b32 m0, s75
	v_and_b32_e32 v3, 15, v0
	global_load_lds_dwordx4 v[4:5], off
	v_bfe_u32 v4, v0, 4, 2
	v_lshlrev_b32_e32 v205, 3, v4
	v_lshlrev_b32_e32 v4, 4, v4
	v_lshlrev_b32_e32 v6, 2, v0
	v_lshlrev_b32_e32 v7, 6, v0
	s_movk_i32 s4, 0x3c0
	v_lshl_or_b32 v5, v3, 6, v4
	v_and_b32_e32 v6, 32, v6
	v_and_or_b32 v4, v7, s4, v4
	s_cmpk_lt_u32 s11, 0x100
	v_bitop3_b32 v5, v5, s6, v6 bitop3:0xde
	v_bitop3_b32 v4, s7, v4, v6 bitop3:0xf6
	s_waitcnt vmcnt(6)
	v_and_b32_e32 v6, 31, v0
	v_cmp_eq_u32_e64 s[4:5], 0, v2
	s_cselect_b64 s[18:19], -1, 0
	v_and_b32_e32 v2, 16, v0
	s_add_i32 s6, 0, 0x20140
	v_or3_b32 v219, s20, v3, v2
	v_lshl_add_u32 v221, v6, 2, s6
	s_add_i32 s6, 0, 0x20400
	v_and_b32_e32 v207, 16, v205
	v_or_b32_e32 v220, 32, v219
	v_mov_b32_e32 v222, s6
	s_mov_b64 s[20:21], 0x2000
	s_mov_b32 s76, 0x401c62bf
	s_mov_b32 s77, 0xc3e00000
	v_add_u32_e32 v223, 0, v4
	v_add_u32_e32 v224, 0, v5
	v_mov_b32_e32 v225, 0xc05083aa
	v_mov_b32_e32 v226, 0x43e00000
	s_barrier
	s_branch .LBB0_1303

;     __device__ __forceinline__ bool next(int i, Unit& u) const { const int L = i * G + c; if (L >= nunits) return false; u.e = L / nPM; u.pm = L % nPM; u.pn = 0; u.rb = 0; u.nvalid = 256; return true; }
;     ...
;         const bool has_next = S.next(ui + 1, nxt);
;         const char* nA = has_next ? S.a_ptr(nxt) : cA; const char* nB = has_next ? S.b_ptr(nxt) : cB;
;         rotn = has_next ? S.krot(nxt, nt) : rotc;
;         const bool full = !HALFU || cur.nvalid > 128;
; #pragma unroll 1
;         for (int t = 0; t < nt; t += 2) {
;             const bool last = (t == nt - 2);
;             const bool fin = last && !has_next;
;             const char* a1 = cA + PG8_KOFS(rotc, t + 1);
;             const size_t k2 = last ? PG8_KOFS(rotn, 0) : PG8_KOFS(rotc, t + 2), k3 = last ? PG8_KOFS(rotn, 1) : PG8_KOFS(rotc, t + 3);
;             const char* a2 = (last ? nA : cA) + k2; const char* b2 = (last ? nB : cB) + k2;
;             const char* a3 = (last ? nA : cA) + k3; const char* b3 = (last ? nB : cB) + k3;
;             unsigned o2[2][2];
; #pragma unroll
;             for (int h = 0; h < 2; ++h)
; #pragma unroll
;                 for (int i = 0; i < 2; ++i) o2[h][i] = gcur[h][i];
;             if constexpr (GATHER) {
;                 if (t == 0 && has_next) {
; #pragma unroll
;                     for (int h = 0; h < 2; ++h)
; #pragma unroll
;                         for (int i = 0; i < 2; ++i) gnxt[h][i] = S.a_rowoff(nxt, h * HALF + rowA[i]) + colA[i];
;                 }
;                 if (last && has_next) {
;     __device__ __forceinline__ unsigned a_rowoff(const Unit& u, int r) const { const int idx = (r < u.nvalid) ? (u.rb * 256 + r) : 0; const int tok = ltok[(size_t)u.e * LCAP + idx]; return (unsigned)tok * (unsigned)D; }
;     __device__ __forceinline__ int krot(const Unit& u, int nt) const { return (2 * u.rb + u.pn) % nt; }
.LBB0_1307:
	s_lshl_b32 s8, s78, 1
	s_add_i32 s8, s24, s8
	s_ashr_i32 s9, s8, 31
	s_lshr_b32 s9, s9, 28
	s_add_i32 s9, s8, s9
	s_and_b32 s9, s9, -16
	s_sub_i32 s25, s8, s9
	s_and_b64 s[8:9], s[40:41], exec
	s_cselect_b32 s42, s25, s38
	s_cmpk_gt_i32 s10, 0x80
	s_cselect_b64 s[44:45], -1, 0
	s_ashr_i32 s43, s42, 31
	s_xor_b64 s[46:47], s[40:41], -1
	s_lshl_b64 s[8:9], s[42:43], 7
	s_add_u32 s8, s8, 0x80
	s_addc_u32 s9, s9, 0
	s_cmp_lt_i32 s42, 15
	s_cselect_b32 s29, s9, 0
	s_cselect_b32 s43, s8, 0
	s_lshl_b32 s10, s78, 8
	v_or_b32_e32 v2, s10, v1
	v_cmp_gt_i32_e32 vcc, s79, v1
	v_or_b32_e32 v4, s10, v195
	v_or_b32_e32 v6, s10, v216
	v_cndmask_b32_e32 v2, 0, v2, vcc
	v_cmp_gt_i32_e32 vcc, s79, v195
	s_lshl_b64 s[8:9], s[22:23], 16
	v_or_b32_e32 v8, s10, v217
	v_cndmask_b32_e32 v4, 0, v4, vcc
	v_cmp_gt_i32_e32 vcc, s79, v216
	s_add_u32 s8, s49, s8
	v_cndmask_b32_e32 v6, 0, v6, vcc
	v_cmp_gt_i32_e32 vcc, s79, v217
	v_ashrrev_i32_e32 v3, 31, v2
	v_cndmask_b32_e32 v8, 0, v8, vcc
	v_ashrrev_i32_e32 v5, 31, v4
	v_ashrrev_i32_e32 v7, 31, v6
	v_ashrrev_i32_e32 v9, 31, v8
	s_addc_u32 s9, s58, s9
	v_mov_b32_e32 v203, v201
	v_lshl_add_u64 v[208:209], v[2:3], 2, s[8:9]
	v_lshl_add_u64 v[210:211], v[4:5], 2, s[8:9]
	v_lshl_add_u64 v[212:213], v[6:7], 2, s[8:9]
	v_lshl_add_u64 v[214:215], v[8:9], 2, s[8:9]
	s_mov_b32 s23, -2
	v_mov_b32_e32 v230, v202
	v_mov_b32_e32 v229, v200
	v_mov_b32_e32 v228, v204
	v_mov_b32_e32 v227, v206
	s_cmp_lt_u32 s67, 2
	s_cbranch_scc1 .Lp9_noR
	s_and_b64 vcc, exec, s[2:3]
	s_cbranch_vccz .Lp9_noR
	s_barrier

; #define PG8_STAGE2(bufoff, gbase, o0, o1) do { \
;         __builtin_amdgcn_global_load_lds((const unsigned*)((const char*)(gbase) + (o0)), (PG8_LAS unsigned*)(lds + (bufoff) + ldsw), 16, 0, 0); \
;         __builtin_amdgcn_global_load_lds((const unsigned*)((const char*)(gbase) + (o1)), (PG8_LAS unsigned*)(lds + (bufoff) + ldsw + 8192), 16, 0, 0); } while (0)
; #define PG8_STAGE_B(bufoff, gbase) PG8_STAGE2(bufoff, gbase, voffB[0], voffB[1])
; #define PG8_WAIT_V(n) asm volatile("s_waitcnt vmcnt(" #n ")" ::: "memory")
; #define PG8_WAIT_L(n) asm volatile("s_waitcnt lgkmcnt(" #n ")" ::: "memory")
; #define PG8_BAR __builtin_amdgcn_s_barrier()
; #define PG8_SCHED __builtin_amdgcn_sched_barrier(0)
;     ...
;             PG8_LDB(B0, 0, 0); PG8_LDB(B1, 0, 1); PG8_SCHED; PG8_LDA(At, 0, 0); PG8_STAGE2(PG8_SA(1, 1), a1 + hstepA, gcur[1][0], gcur[1][1]);
;             PG8_WAIT_V(8); PG8_WAIT_L(0); PG8_BAR; PG8_MMA(0, 0, At, B0); PG8_MMA(0, 1, At, B1); PG8_BAR; PG8_SCHED;
;             if (full) { PG8_LDA(At, 0, 1); }
;             if (!fin) { PG8_STAGE_B(PG8_SB(0, 0), b2); PG8_STAGE_B(PG8_SB(0, 1), b2 + hstepB); PG8_STAGE2(PG8_SA(0, 0), a2, o2[0][0], o2[0][1]); PG8_WAIT_V(8); }
;             else { PG8_WAIT_V(2); }
;             PG8_WAIT_L(0); PG8_BAR; if (full) { PG8_MMA(1, 0, At, B0); PG8_MMA(1, 1, At, B1); } PG8_BAR; PG8_SCHED;
.Lp9_nognxt:
	v_add_u32_e32 v238, 0x10000, v223
	s_add_i32 s82, s38, s23
	s_add_i32 s84, s82, 3
	s_and_b32 s84, s84, 15
	s_lshl_b32 s84, s84, 7
	s_add_u32 s8, s59, s84
	s_addc_u32 s9, s60, 0
	ds_read_b128 v[10:13], v238
	ds_read_b128 v[14:17], v238 offset:1024
	ds_read_b128 v[26:29], v238 offset:2048
	ds_read_b128 v[30:33], v238 offset:3072
	ds_read_b128 v[2:5], v238 offset:16384
	ds_read_b128 v[6:9], v238 offset:17408
	ds_read_b128 v[18:21], v238 offset:18432
	ds_read_b128 v[22:25], v238 offset:19456
	ds_read_b128 v[34:37], v224
	ds_read_b128 v[38:41], v224 offset:1024
	ds_read_b128 v[42:45], v224 offset:2048
	ds_read_b128 v[46:49], v224 offset:3072
	ds_read_b128 v[50:53], v224 offset:4096
	ds_read_b128 v[54:57], v224 offset:5120
	ds_read_b128 v[58:61], v224 offset:6144
	ds_read_b128 v[62:65], v224 offset:7168
	s_add_i32 m0, s31, 0xc000
	s_nop 0
	global_load_lds_dwordx4 v200, s[8:9]
	s_add_i32 m0, s31, 0xe000
	s_nop 0
	global_load_lds_dwordx4 v202, s[8:9]
	s_waitcnt vmcnt(8)
	s_waitcnt lgkmcnt(0)
	s_barrier
	s_setprio 1
	s_nop 1
	v_mfma_f32_16x16x128_f8f6f4 v[190:193], v[10:17], v[34:41], 0
	v_mfma_f32_16x16x128_f8f6f4 v[186:189], v[26:33], v[34:41], 0
	v_mfma_f32_16x16x128_f8f6f4 v[174:177], v[10:17], v[42:49], 0
	v_mfma_f32_16x16x128_f8f6f4 v[170:173], v[26:33], v[42:49], 0
	v_mfma_f32_16x16x128_f8f6f4 v[158:161], v[10:17], v[50:57], 0
	v_mfma_f32_16x16x128_f8f6f4 v[154:157], v[26:33], v[50:57], 0
	v_mfma_f32_16x16x128_f8f6f4 v[142:145], v[10:17], v[58:65], 0
	v_mfma_f32_16x16x128_f8f6f4 v[138:141], v[26:33], v[58:65], 0
	v_mfma_f32_16x16x128_f8f6f4 v[182:185], v[2:9], v[34:41], 0
	v_mfma_f32_16x16x128_f8f6f4 v[178:181], v[18:25], v[34:41], 0
	v_mfma_f32_16x16x128_f8f6f4 v[166:169], v[2:9], v[42:49], 0
	v_mfma_f32_16x16x128_f8f6f4 v[162:165], v[18:25], v[42:49], 0
	v_mfma_f32_16x16x128_f8f6f4 v[150:153], v[2:9], v[50:57], 0
	v_mfma_f32_16x16x128_f8f6f4 v[146:149], v[18:25], v[50:57], 0
	v_mfma_f32_16x16x128_f8f6f4 v[134:137], v[2:9], v[58:65], 0
	v_mfma_f32_16x16x128_f8f6f4 v[130:133], v[18:25], v[58:65], 0
	s_setprio 0
	s_barrier
	s_add_i32 s84, s82, 4
	s_and_b32 s84, s84, 15
	s_lshl_b32 s84, s84, 7
	ds_read_b128 v[34:37], v224 offset:16384
	ds_read_b128 v[38:41], v224 offset:17408
	ds_read_b128 v[42:45], v224 offset:18432
	ds_read_b128 v[46:49], v224 offset:19456
	ds_read_b128 v[50:53], v224 offset:20480
	ds_read_b128 v[54:57], v224 offset:21504
	ds_read_b128 v[58:61], v224 offset:22528
	ds_read_b128 v[62:65], v224 offset:23552
	s_add_u32 s52, s36, s84
	s_addc_u32 s53, s37, 0
	s_add_u32 s56, s52, 0x40000
	s_addc_u32 s57, s53, 0
	s_add_u32 s14, s59, s84
	s_addc_u32 s15, s60, 0
	s_mov_b32 m0, s39
	s_nop 0
	global_load_lds_dwordx4 v196, s[52:53]
	s_mov_b32 m0, s61
	s_nop 0
	global_load_lds_dwordx4 v198, s[52:53]
	s_mov_b32 m0, s62
	s_nop 0
	global_load_lds_dwordx4 v196, s[56:57]
	s_mov_b32 m0, s63
	s_nop 0
	global_load_lds_dwordx4 v198, s[56:57]
	s_mov_b32 m0, s31
	s_nop 0
	global_load_lds_dwordx4 v206, s[14:15]
	s_mov_b32 m0, s64
	s_nop 0
	global_load_lds_dwordx4 v204, s[14:15]
	s_waitcnt vmcnt(8)
	s_waitcnt lgkmcnt(0)
	s_barrier
	s_setprio 1
	s_nop 1
	v_mfma_f32_16x16x128_f8f6f4 v[126:129], v[10:17], v[34:41], 0
	v_mfma_f32_16x16x128_f8f6f4 v[122:125], v[26:33], v[34:41], 0
	v_mfma_f32_16x16x128_f8f6f4 v[110:113], v[10:17], v[42:49], 0
	v_mfma_f32_16x16x128_f8f6f4 v[106:109], v[26:33], v[42:49], 0
	v_mfma_f32_16x16x128_f8f6f4 v[94:97], v[10:17], v[50:57], 0
	v_mfma_f32_16x16x128_f8f6f4 v[90:93], v[26:33], v[50:57], 0
	v_mfma_f32_16x16x128_f8f6f4 v[78:81], v[10:17], v[58:65], 0
	v_mfma_f32_16x16x128_f8f6f4 v[74:77], v[26:33], v[58:65], 0
	v_mfma_f32_16x16x128_f8f6f4 v[118:121], v[2:9], v[34:41], 0
	v_mfma_f32_16x16x128_f8f6f4 v[114:117], v[18:25], v[34:41], 0
	v_mfma_f32_16x16x128_f8f6f4 v[102:105], v[2:9], v[42:49], 0
	v_mfma_f32_16x16x128_f8f6f4 v[98:101], v[18:25], v[42:49], 0
	v_mfma_f32_16x16x128_f8f6f4 v[86:89], v[2:9], v[50:57], 0
	v_mfma_f32_16x16x128_f8f6f4 v[82:85], v[18:25], v[50:57], 0
	v_mfma_f32_16x16x128_f8f6f4 v[70:73], v[2:9], v[58:65], 0
	v_mfma_f32_16x16x128_f8f6f4 v[66:69], v[18:25], v[58:65], 0
	s_setprio 0
	s_barrier
; #define PG8_STAGE2(bufoff, gbase, o0, o1) do { \
;         __builtin_amdgcn_global_load_lds((const unsigned*)((const char*)(gbase) + (o0)), (PG8_LAS unsigned*)(lds + (bufoff) + ldsw), 16, 0, 0); \
;         __builtin_amdgcn_global_load_lds((const unsigned*)((const char*)(gbase) + (o1)), (PG8_LAS unsigned*)(lds + (bufoff) + ldsw + 8192), 16, 0, 0); } while (0)
; #define PG8_STAGE_B(bufoff, gbase) PG8_STAGE2(bufoff, gbase, voffB[0], voffB[1])
; #define PG8_WAIT_V(n) asm volatile("s_waitcnt vmcnt(" #n ")" ::: "memory")
; #define PG8_WAIT_L(n) asm volatile("s_waitcnt lgkmcnt(" #n ")" ::: "memory")
; #define PG8_BAR __builtin_amdgcn_s_barrier()
; #define PG8_SCHED __builtin_amdgcn_sched_barrier(0)
;     ...
;             PG8_LDB(B0, 1, 0); PG8_LDB(B1, 1, 1); PG8_SCHED; PG8_LDA(At, 1, 0);
;             if (!fin) { PG8_STAGE2(PG8_SA(0, 1), a2 + hstepA, o2[1][0], o2[1][1]); PG8_WAIT_V(8); } else { PG8_WAIT_V(0); }
;             PG8_WAIT_L(0); PG8_BAR; PG8_MMA(0, 0, At, B0); PG8_MMA(0, 1, At, B1); PG8_BAR; PG8_SCHED;
;             if (full) { PG8_LDA(At, 1, 1); }
;             if (!fin) { PG8_STAGE_B(PG8_SB(1, 0), b3); PG8_STAGE_B(PG8_SB(1, 1), b3 + hstepB); PG8_STAGE2(PG8_SA(1, 0), a3, o2[0][0], o2[0][1]); PG8_WAIT_V(8); }
;             PG8_WAIT_L(0); PG8_BAR; if (full) { PG8_MMA(1, 0, At, B0); PG8_MMA(1, 1, At, B1); } PG8_BAR; PG8_SCHED;
	s_add_i32 s84, s82, 5
	s_and_b32 s84, s84, 15
	s_lshl_b32 s84, s84, 7
	ds_read_b128 v[50:53], v238 offset:32768
	ds_read_b128 v[54:57], v238 offset:33792
	ds_read_b128 v[58:61], v238 offset:34816
	ds_read_b128 v[62:65], v238 offset:35840
	ds_read_b128 v[2:5], v238 offset:49152
	ds_read_b128 v[6:9], v238 offset:50176
	ds_read_b128 v[10:13], v238 offset:51200
	ds_read_b128 v[14:17], v238 offset:52224
	ds_read_b128 v[18:21], v224 offset:32768
	ds_read_b128 v[22:25], v224 offset:33792
	ds_read_b128 v[26:29], v224 offset:34816
	ds_read_b128 v[30:33], v224 offset:35840
	ds_read_b128 v[34:37], v224 offset:36864
	ds_read_b128 v[38:41], v224 offset:37888
	ds_read_b128 v[42:45], v224 offset:38912
	ds_read_b128 v[46:49], v224 offset:39936
	s_mov_b32 m0, s65
	s_nop 0
	global_load_lds_dwordx4 v200, s[14:15]
	s_mov_b32 m0, s66
	s_nop 0
	global_load_lds_dwordx4 v202, s[14:15]
	s_waitcnt vmcnt(8)
	s_waitcnt lgkmcnt(0)
	s_barrier
	s_setprio 1
	s_nop 1
	v_mfma_f32_16x16x128_f8f6f4 v[190:193], v[50:57], v[18:25], v[190:193]
	v_mfma_f32_16x16x128_f8f6f4 v[186:189], v[58:65], v[18:25], v[186:189]
	v_mfma_f32_16x16x128_f8f6f4 v[174:177], v[50:57], v[26:33], v[174:177]
	v_mfma_f32_16x16x128_f8f6f4 v[170:173], v[58:65], v[26:33], v[170:173]
	v_mfma_f32_16x16x128_f8f6f4 v[158:161], v[50:57], v[34:41], v[158:161]
	v_mfma_f32_16x16x128_f8f6f4 v[154:157], v[58:65], v[34:41], v[154:157]
	v_mfma_f32_16x16x128_f8f6f4 v[142:145], v[50:57], v[42:49], v[142:145]
	v_mfma_f32_16x16x128_f8f6f4 v[138:141], v[58:65], v[42:49], v[138:141]
	v_mfma_f32_16x16x128_f8f6f4 v[182:185], v[2:9], v[18:25], v[182:185]
	v_mfma_f32_16x16x128_f8f6f4 v[178:181], v[10:17], v[18:25], v[178:181]
	v_mfma_f32_16x16x128_f8f6f4 v[166:169], v[2:9], v[26:33], v[166:169]
	v_mfma_f32_16x16x128_f8f6f4 v[162:165], v[10:17], v[26:33], v[162:165]
	v_mfma_f32_16x16x128_f8f6f4 v[150:153], v[2:9], v[34:41], v[150:153]
	v_mfma_f32_16x16x128_f8f6f4 v[146:149], v[10:17], v[34:41], v[146:149]
	v_mfma_f32_16x16x128_f8f6f4 v[134:137], v[2:9], v[42:49], v[134:137]
	v_mfma_f32_16x16x128_f8f6f4 v[130:133], v[10:17], v[42:49], v[130:133]
	s_setprio 0
	s_barrier
	ds_read_b128 v[18:21], v224 offset:49152
	ds_read_b128 v[22:25], v224 offset:50176
	ds_read_b128 v[26:29], v224 offset:51200
	ds_read_b128 v[30:33], v224 offset:52224
	ds_read_b128 v[34:37], v224 offset:53248
	ds_read_b128 v[38:41], v224 offset:54272
	ds_read_b128 v[42:45], v224 offset:55296
	ds_read_b128 v[46:49], v224 offset:56320
	s_add_u32 s10, s36, s84
	s_addc_u32 s11, s37, 0
	s_add_u32 s34, s10, 0x40000
	s_addc_u32 s35, s11, 0
	s_add_u32 s90, s59, s84
	s_addc_u32 s91, s60, 0
	s_mov_b32 m0, s70
	s_nop 0
	global_load_lds_dwordx4 v196, s[10:11]
	s_mov_b32 m0, s71
	s_nop 0
	global_load_lds_dwordx4 v198, s[10:11]
	s_mov_b32 m0, s74
	s_nop 0
	global_load_lds_dwordx4 v196, s[34:35]
	s_mov_b32 m0, s75
	s_nop 0
	global_load_lds_dwordx4 v198, s[34:35]
	s_mov_b32 m0, s72
	s_nop 0
	global_load_lds_dwordx4 v206, s[90:91]
	s_mov_b32 m0, s73
	s_nop 0
	global_load_lds_dwordx4 v204, s[90:91]
	s_waitcnt vmcnt(8)
	s_waitcnt lgkmcnt(0)
	s_barrier
	s_setprio 1
	s_nop 1
	v_mfma_f32_16x16x128_f8f6f4 v[126:129], v[50:57], v[18:25], v[126:129]
	v_mfma_f32_16x16x128_f8f6f4 v[122:125], v[58:65], v[18:25], v[122:125]
	v_mfma_f32_16x16x128_f8f6f4 v[110:113], v[50:57], v[26:33], v[110:113]
	v_mfma_f32_16x16x128_f8f6f4 v[106:109], v[58:65], v[26:33], v[106:109]
	v_mfma_f32_16x16x128_f8f6f4 v[94:97], v[50:57], v[34:41], v[94:97]
	v_mfma_f32_16x16x128_f8f6f4 v[90:93], v[58:65], v[34:41], v[90:93]
	v_mfma_f32_16x16x128_f8f6f4 v[78:81], v[50:57], v[42:49], v[78:81]
	v_mfma_f32_16x16x128_f8f6f4 v[74:77], v[58:65], v[42:49], v[74:77]
	v_mfma_f32_16x16x128_f8f6f4 v[118:121], v[2:9], v[18:25], v[118:121]
	v_mfma_f32_16x16x128_f8f6f4 v[114:117], v[10:17], v[18:25], v[114:117]
	v_mfma_f32_16x16x128_f8f6f4 v[102:105], v[2:9], v[26:33], v[102:105]
	v_mfma_f32_16x16x128_f8f6f4 v[98:101], v[10:17], v[26:33], v[98:101]
	v_mfma_f32_16x16x128_f8f6f4 v[86:89], v[2:9], v[34:41], v[86:89]
	v_mfma_f32_16x16x128_f8f6f4 v[82:85], v[10:17], v[34:41], v[82:85]
	v_mfma_f32_16x16x128_f8f6f4 v[70:73], v[2:9], v[42:49], v[70:73]
	v_mfma_f32_16x16x128_f8f6f4 v[66:69], v[10:17], v[42:49], v[66:69]
	s_setprio 0
	s_barrier
	s_add_i32 s23, s23, 2

;     ...
; #pragma unroll
;         for (int a = 0; a < 2; ++a)
; #pragma unroll
;             for (int b = 0; b < 2; ++b)
; #pragma unroll
;                 for (int m = 0; m < 4; ++m)
; #pragma unroll
;                     for (int n = 0; n < 2; ++n) acc[a][b][m][n] = (f32x4){0.f, 0.f, 0.f, 0.f};
.Lp9_zero:
	v_mov_b32_e32 v68, v201
	v_mov_b32_e32 v69, v201
	v_mov_b32_e32 v66, v201
	v_mov_b32_e32 v67, v201
	v_mov_b32_e32 v130, 0
	v_mov_b64_e32 v[72:73], v[68:69]
	v_mov_b64_e32 v[84:85], v[68:69]
	v_mov_b64_e32 v[88:89], v[68:69]
	v_mov_b64_e32 v[100:101], v[68:69]
	v_mov_b64_e32 v[104:105], v[68:69]
	v_mov_b64_e32 v[116:117], v[68:69]
	v_mov_b64_e32 v[120:121], v[68:69]
	v_mov_b64_e32 v[76:77], v[68:69]
	v_mov_b64_e32 v[80:81], v[68:69]
	v_mov_b64_e32 v[92:93], v[68:69]
	v_mov_b64_e32 v[96:97], v[68:69]
	v_mov_b64_e32 v[108:109], v[68:69]
	v_mov_b64_e32 v[112:113], v[68:69]
	v_mov_b64_e32 v[124:125], v[68:69]
	v_mov_b64_e32 v[128:129], v[68:69]
	v_mov_b64_e32 v[70:71], v[66:67]
	v_mov_b64_e32 v[82:83], v[66:67]
	v_mov_b64_e32 v[86:87], v[66:67]
	v_mov_b64_e32 v[98:99], v[66:67]
	v_mov_b64_e32 v[102:103], v[66:67]
	v_mov_b64_e32 v[114:115], v[66:67]
	v_mov_b64_e32 v[118:119], v[66:67]
	v_mov_b64_e32 v[74:75], v[66:67]
	v_mov_b64_e32 v[78:79], v[66:67]
	v_mov_b64_e32 v[90:91], v[66:67]
	v_mov_b64_e32 v[94:95], v[66:67]
	v_mov_b64_e32 v[106:107], v[66:67]
	v_mov_b64_e32 v[110:111], v[66:67]
	v_mov_b64_e32 v[122:123], v[66:67]
	v_mov_b64_e32 v[126:127], v[66:67]
	v_mov_b32_e32 v131, v130
	v_mov_b32_e32 v132, v130
	v_mov_b32_e32 v133, v130
	v_mov_b32_e32 v134, v130
	v_mov_b32_e32 v135, v130
	v_mov_b32_e32 v136, v130
	v_mov_b32_e32 v137, v130
	v_mov_b32_e32 v146, v130
	v_mov_b32_e32 v147, v130
	v_mov_b32_e32 v148, v130
	v_mov_b32_e32 v149, v130
	v_mov_b32_e32 v150, v130
	v_mov_b32_e32 v151, v130
	v_mov_b32_e32 v152, v130
	v_mov_b32_e32 v153, v130
	v_mov_b32_e32 v162, v130
	v_mov_b32_e32 v163, v130
	v_mov_b32_e32 v164, v130
	v_mov_b32_e32 v165, v130
	v_mov_b32_e32 v166, v130
	v_mov_b32_e32 v167, v130
	v_mov_b32_e32 v168, v130
	v_mov_b32_e32 v169, v130
	v_mov_b32_e32 v178, v130
	v_mov_b32_e32 v179, v130
	v_mov_b32_e32 v180, v130
	v_mov_b32_e32 v181, v130
	v_mov_b32_e32 v182, v130
	v_mov_b32_e32 v183, v130
	v_mov_b32_e32 v184, v130
	v_mov_b32_e32 v185, v130
	v_mov_b32_e32 v138, v130
	v_mov_b32_e32 v139, v130
	v_mov_b32_e32 v140, v130
	v_mov_b32_e32 v141, v130
	v_mov_b32_e32 v142, v130
	v_mov_b32_e32 v143, v130
	v_mov_b32_e32 v144, v130
	v_mov_b32_e32 v145, v130
	v_mov_b32_e32 v154, v130
	v_mov_b32_e32 v155, v130
	v_mov_b32_e32 v156, v130
	v_mov_b32_e32 v157, v130
	v_mov_b32_e32 v158, v130
	v_mov_b32_e32 v159, v130
	v_mov_b32_e32 v160, v130
	v_mov_b32_e32 v161, v130
	v_mov_b32_e32 v170, v130
	v_mov_b32_e32 v171, v130
	v_mov_b32_e32 v172, v130
	v_mov_b32_e32 v173, v130
	v_mov_b32_e32 v174, v130
	v_mov_b32_e32 v175, v130
	v_mov_b32_e32 v176, v130
	v_mov_b32_e32 v177, v130
	v_mov_b32_e32 v186, v130
	v_mov_b32_e32 v187, v130
	v_mov_b32_e32 v188, v130
	v_mov_b32_e32 v189, v130
	v_mov_b32_e32 v190, v130
	v_mov_b32_e32 v191, v130
	v_mov_b32_e32 v192, v130
	v_mov_b32_e32 v193, v130
	s_branch .LBB0_1309

; __device__ __forceinline__ float sigmoidf_(float x) { return __builtin_amdgcn_rcpf(1.0f + __builtin_amdgcn_exp2f(-1.44269504089f * x)); }
;     __device__ __forceinline__ void operator()(EPI_ARGS) const {
;         const int j0 = u.pn * 128 + wc * 32 + 8 * fq; const float* bb = b1 + (size_t)u.e * 2 * FE;
;         const f32x4 ba0 = *(const f32x4*)(bb + j0), ba1 = *(const f32x4*)(bb + j0 + 4), bl0 = *(const f32x4*)(bb + FE + j0), bl1 = *(const f32x4*)(bb + FE + j0 + 4);
;         const int j0q = u.pn * 128 + wc * 32 + 8 * (fq & ~1);
; #pragma unroll
;         for (int ai = 0; ai < 2; ++ai)
; #pragma unroll
;             for (int mp = 0; mp < 2; ++mp) { unsigned px[2], py[2];
; #pragma unroll
;                 for (int h = 0; h < 2; ++h) { const int m = 2 * mp + h;
;                     const f32x4 a0 = acc[ai][0][m][0] * 0.03125f + ba0, a1 = acc[ai][0][m][1] * 0.03125f + ba1, l0 = acc[ai][1][m][0] * 0.03125f + bl0, l1 = acc[ai][1][m][1] * 0.03125f + bl1;
;                     float o[8];
; #pragma unroll
;                     for (int j = 0; j < 4; ++j) { const float g0 = fminf(a0[j], 7.0f), g1 = fminf(a1[j], 7.0f), x0 = fminf(fmaxf(l0[j], -7.0f), 7.0f), x1 = fminf(fmaxf(l1[j], -7.0f), 7.0f);
;                         o[j] = g0 * sigmoidf_(1.702f * g0) * (x0 + 1.0f); o[4 + j] = g1 * sigmoidf_(1.702f * g1) * (x1 + 1.0f); }
;                     px[h] = pk4_fp8(o[0], o[1], o[2], o[3]); py[h] = pk4_fp8(o[4], o[5], o[6], o[7]); }
.LBB0_1334:
	s_lshl_b32 s8, s30, 7
	s_or_b32 s10, s8, s69
	s_lshl_b32 s8, s81, 8
	s_nop 15
	v_mul_f32_e32 v10, 0xc01d265f, v240
	v_mul_f32_e32 v11, 0xc01d265f, v241
	v_mul_f32_e32 v12, 0xc01d265f, v242
	v_mul_f32_e32 v13, 0xc01d265f, v243
	v_mul_f32_e32 v6, 0xc01d265f, v244
	v_mul_f32_e32 v7, 0xc01d265f, v245
	v_mul_f32_e32 v8, 0xc01d265f, v246
	v_mul_f32_e32 v9, 0xc01d265f, v247
	v_add_f32_e32 v14, 1.0, v248
	v_mul_f32_e32 v14, 0xbed083aa, v14
	v_add_f32_e32 v15, 1.0, v249
	v_mul_f32_e32 v15, 0xbed083aa, v15
	v_add_f32_e32 v16, 1.0, v250
	v_mul_f32_e32 v16, 0xbed083aa, v16
	v_add_f32_e32 v17, 1.0, v251
	v_mul_f32_e32 v17, 0xbed083aa, v17
	v_add_f32_e32 v2, 1.0, v252
	v_mul_f32_e32 v2, 0xbed083aa, v2
	v_add_f32_e32 v3, 1.0, v253
	v_mul_f32_e32 v3, 0xbed083aa, v3
	v_add_f32_e32 v4, 1.0, v255
	v_mul_f32_e32 v4, 0xbed083aa, v4
	v_add_f32_e32 v5, 1.0, v239
	v_mul_f32_e32 v5, 0xbed083aa, v5
	s_waitcnt lgkmcnt(0)
	v_or_b32_e32 v18, s10, v207
	v_ashrrev_i32_e32 v19, 31, v18
	s_and_b64 vcc, exec, s[6:7]
	s_mov_b64 s[6:7], -1
	v_fmamk_f32 v20, v190, 0xbd9d265f, v10
	v_max_f32_e32 v20, 0xc1898193, v20
	v_exp_f32_e32 v30, v20
	v_fmamk_f32 v21, v186, 0xbd9d265f, v6
	v_max_f32_e32 v21, 0xc1898193, v21
	v_add_f32_e32 v30, 1.0, v30
	v_exp_f32_e32 v31, v21
	v_rcp_f32_e32 v30, v30
	v_fmamk_f32 v22, v191, 0xbd9d265f, v11
	v_fmamk_f32 v23, v187, 0xbd9d265f, v7
	v_fmamk_f32 v27, v189, 0xbd9d265f, v9
	v_max_f32_e32 v22, 0xc1898193, v22
	v_max_f32_e32 v23, 0xc1898193, v23
	v_max_f32_e32 v27, 0xc1898193, v27
	v_add_f32_e32 v31, 1.0, v31
	v_mul_f32_e32 v20, v20, v30
	v_exp_f32_e32 v34, v22
	v_rcp_f32_e32 v31, v31
	v_fmamk_f32 v25, v188, 0xbd9d265f, v8
	v_exp_f32_e32 v35, v23
	v_exp_f32_e32 v30, v27
	v_max_f32_e32 v25, 0xc1898193, v25
	v_fmamk_f32 v29, v178, 0xbc5083aa, v2
	v_fmamk_f32 v24, v192, 0xbd9d265f, v12
	v_fmamk_f32 v26, v193, 0xbd9d265f, v13
	v_med3_f32 v29, v29, s76, v225
	v_max_f32_e32 v24, 0xc1898193, v24
	v_max_f32_e32 v26, 0xc1898193, v26
	v_add_f32_e32 v34, 1.0, v34
	v_mul_f32_e32 v21, v21, v31
	v_fmamk_f32 v28, v182, 0xbc5083aa, v14
	v_exp_f32_e32 v39, v25
	v_add_f32_e32 v35, 1.0, v35
	v_rcp_f32_e32 v34, v34
	v_mul_f32_e32 v21, v29, v21
	v_add_f32_e32 v30, 1.0, v30
	v_med3_f32 v28, v28, s76, v225
	v_rcp_f32_e32 v35, v35
	v_rcp_f32_e32 v30, v30
	v_fmamk_f32 v32, v183, 0xbc5083aa, v15
	v_exp_f32_e32 v38, v24
	v_exp_f32_e32 v29, v26
	v_fmamk_f32 v33, v179, 0xbc5083aa, v3
	v_med3_f32 v32, v32, s76, v225
	v_mul_f32_e32 v20, v28, v20
	v_fmamk_f32 v28, v181, 0xbc5083aa, v5
	v_med3_f32 v33, v33, s76, v225
	v_add_f32_e32 v39, 1.0, v39
	v_mul_f32_e32 v22, v22, v34
	v_med3_f32 v28, v28, s76, v225
	v_rcp_f32_e32 v39, v39
	v_mul_f32_e32 v23, v23, v35
	v_mul_f32_e32 v22, v32, v22
	v_mul_f32_e32 v27, v27, v30
	v_add_f32_e32 v38, 1.0, v38
	v_mul_f32_e32 v23, v33, v23
	v_add_f32_e32 v29, 1.0, v29
	v_mul_f32_e32 v27, v28, v27
	v_mov_b32_e32 v28, v22
	v_mov_b32_e32 v22, v201
	v_fmamk_f32 v37, v180, 0xbc5083aa, v4
	v_rcp_f32_e32 v38, v38
	v_rcp_f32_e32 v29, v29
	v_cvt_pk_fp8_f32 v22, v20, v28
	v_mov_b32_e32 v20, v21
	v_mov_b32_e32 v21, v23
	v_mov_b32_e32 v23, v201
	v_med3_f32 v37, v37, s76, v225
	v_cvt_pk_fp8_f32 v23, v20, v21
	v_fmamk_f32 v36, v184, 0xbc5083aa, v16
	v_fmamk_f32 v40, v185, 0xbc5083aa, v17
	v_mul_f32_e32 v25, v25, v39
	v_med3_f32 v36, v36, s76, v225
	v_med3_f32 v40, v40, s76, v225
	v_mul_f32_e32 v25, v37, v25
	v_mul_f32_e32 v24, v24, v38
	v_mul_f32_e32 v26, v26, v29
	v_mul_f32_e32 v24, v36, v24
	v_mul_f32_e32 v26, v40, v26
	v_cvt_pk_fp8_f32 v23, v25, v27 op_sel:[0, 0, 1]
	v_fmamk_f32 v20, v174, 0xbd9d265f, v10
	v_max_f32_e32 v20, 0xc1898193, v20
	v_fmamk_f32 v21, v170, 0xbd9d265f, v6
	v_cvt_pk_fp8_f32 v22, v24, v26 op_sel:[0,0,1]
	v_max_f32_e32 v21, 0xc1898193, v21
	v_exp_f32_e32 v26, v20
	v_exp_f32_e32 v27, v21
	v_fmamk_f32 v24, v166, 0xbc5083aa, v14
	v_add_f32_e32 v26, 1.0, v26
	v_rcp_f32_e32 v26, v26
	v_add_f32_e32 v27, 1.0, v27
	v_rcp_f32_e32 v27, v27
	v_med3_f32 v24, v24, s76, v225
	v_fmamk_f32 v25, v162, 0xbc5083aa, v2
	v_med3_f32 v25, v25, s76, v225
	v_mul_f32_e32 v20, v20, v26
	v_mul_f32_e32 v20, v24, v20
	v_mul_f32_e32 v21, v21, v27
	v_mul_f32_e32 v21, v25, v21
	v_fmamk_f32 v24, v175, 0xbd9d265f, v11
	v_max_f32_e32 v24, 0xc1898193, v24
	v_fmamk_f32 v25, v171, 0xbd9d265f, v7
	v_max_f32_e32 v25, 0xc1898193, v25
	v_exp_f32_e32 v28, v24
	v_exp_f32_e32 v29, v25
	v_fmamk_f32 v26, v167, 0xbc5083aa, v15
	v_add_f32_e32 v28, 1.0, v28
	v_rcp_f32_e32 v28, v28
	v_add_f32_e32 v29, 1.0, v29
	v_rcp_f32_e32 v29, v29
	v_med3_f32 v26, v26, s76, v225
	v_fmamk_f32 v27, v163, 0xbc5083aa, v3
	v_med3_f32 v27, v27, s76, v225
	v_mul_f32_e32 v24, v24, v28
	v_mul_f32_e32 v24, v26, v24
	v_mul_f32_e32 v25, v25, v29
	v_mul_f32_e32 v25, v27, v25
	v_fmamk_f32 v26, v176, 0xbd9d265f, v12
	v_max_f32_e32 v26, 0xc1898193, v26
	v_fmamk_f32 v27, v172, 0xbd9d265f, v8
	v_max_f32_e32 v27, 0xc1898193, v27
	v_exp_f32_e32 v30, v26
	v_exp_f32_e32 v31, v27
	v_fmamk_f32 v28, v168, 0xbc5083aa, v16
	v_add_f32_e32 v30, 1.0, v30
	v_rcp_f32_e32 v30, v30
	v_add_f32_e32 v31, 1.0, v31
	v_rcp_f32_e32 v31, v31
	v_med3_f32 v28, v28, s76, v225
	v_fmamk_f32 v29, v164, 0xbc5083aa, v4
	v_med3_f32 v29, v29, s76, v225
	v_mul_f32_e32 v26, v26, v30
	v_mul_f32_e32 v26, v28, v26
	v_mul_f32_e32 v27, v27, v31
	v_mul_f32_e32 v27, v29, v27
	v_fmamk_f32 v28, v177, 0xbd9d265f, v13
	v_max_f32_e32 v28, 0xc1898193, v28
	v_fmamk_f32 v29, v173, 0xbd9d265f, v9
	v_max_f32_e32 v29, 0xc1898193, v29
	v_exp_f32_e32 v32, v28
	v_exp_f32_e32 v33, v29
	v_fmamk_f32 v30, v169, 0xbc5083aa, v17
	v_add_f32_e32 v32, 1.0, v32
	v_rcp_f32_e32 v32, v32
	v_add_f32_e32 v33, 1.0, v33
	v_rcp_f32_e32 v33, v33
	v_med3_f32 v30, v30, s76, v225
; __device__ __forceinline__ float sigmoidf_(float x) { return __builtin_amdgcn_rcpf(1.0f + __builtin_amdgcn_exp2f(-1.44269504089f * x)); }
;     __device__ __forceinline__ void operator()(EPI_ARGS) const {
;     ...
;                 for (int h = 0; h < 2; ++h) { const int m = 2 * mp + h;
;                     const f32x4 a0 = acc[ai][0][m][0] * 0.03125f + ba0, a1 = acc[ai][0][m][1] * 0.03125f + ba1, l0 = acc[ai][1][m][0] * 0.03125f + bl0, l1 = acc[ai][1][m][1] * 0.03125f + bl1;
;                     float o[8];
; #pragma unroll
;                     for (int j = 0; j < 4; ++j) { const float g0 = fminf(a0[j], 7.0f), g1 = fminf(a1[j], 7.0f), x0 = fminf(fmaxf(l0[j], -7.0f), 7.0f), x1 = fminf(fmaxf(l1[j], -7.0f), 7.0f);
;                         o[j] = g0 * sigmoidf_(1.702f * g0) * (x0 + 1.0f); o[4 + j] = g1 * sigmoidf_(1.702f * g1) * (x1 + 1.0f); }
;                     px[h] = pk4_fp8(o[0], o[1], o[2], o[3]); py[h] = pk4_fp8(o[4], o[5], o[6], o[7]); }
;                 const u32x4 q = pair16(px[0], py[0], px[1], py[1]);
;                 const int row = u.pm * 256 + ai * 128 + wr * 64 + (2 * mp + (fq & 1)) * 16 + fr;
;                 *(u32x4*)(ACT + (size_t)row * FE + j0q) = q; }
	v_fmamk_f32 v31, v165, 0xbc5083aa, v5
	v_med3_f32 v31, v31, s76, v225
	v_mul_f32_e32 v28, v28, v32
	v_mul_f32_e32 v28, v30, v28
	v_mul_f32_e32 v29, v29, v33
	v_mul_f32_e32 v29, v31, v29
	v_mov_b32_e32 v30, v24
	v_mov_b32_e32 v24, v201
	v_cvt_pk_fp8_f32 v24, v20, v30
	v_mov_b32_e32 v20, v21
	v_mov_b32_e32 v21, v25
	v_mov_b32_e32 v25, v201
	v_cvt_pk_fp8_f32 v25, v20, v21
	v_cvt_pk_fp8_f32 v24, v26, v28 op_sel:[0,0,1]
	v_cvt_pk_fp8_f32 v25, v27, v29 op_sel:[0, 0, 1]
	v_add_u32_e32 v20, s8, v219
	v_ashrrev_i32_e32 v21, 31, v20
	v_lshlrev_b64 v[26:27], 11, v[20:21]
	v_lshl_add_u64 v[26:27], s[16:17], 0, v[26:27]
	v_permlane16_swap_b32_e32 v22, v24
	v_permlane16_swap_b32_e32 v23, v25
	v_lshl_add_u64 v[26:27], v[26:27], 0, v[18:19]
	v_fmamk_f32 v21, v158, 0xbd9d265f, v10
	global_store_dwordx4 v[26:27], v[22:25], off
	v_max_f32_e32 v21, 0xc1898193, v21
	s_nop 0
	v_fmamk_f32 v22, v154, 0xbd9d265f, v6
	v_max_f32_e32 v22, 0xc1898193, v22
	v_exp_f32_e32 v25, v21
	v_exp_f32_e32 v26, v22
	v_fmamk_f32 v23, v150, 0xbc5083aa, v14
	v_add_f32_e32 v25, 1.0, v25
	v_rcp_f32_e32 v25, v25
	v_add_f32_e32 v26, 1.0, v26
	v_rcp_f32_e32 v26, v26
	v_med3_f32 v23, v23, s76, v225
	v_fmamk_f32 v24, v146, 0xbc5083aa, v2
	v_med3_f32 v24, v24, s76, v225
	v_mul_f32_e32 v21, v21, v25
	v_mul_f32_e32 v21, v23, v21
	v_mul_f32_e32 v22, v22, v26
	v_mov_b32_e32 v23, v24
	v_mul_f32_e32 v23, v23, v22
	v_fmamk_f32 v22, v159, 0xbd9d265f, v11
	v_max_f32_e32 v22, 0xc1898193, v22
	v_fmamk_f32 v24, v155, 0xbd9d265f, v7
	v_max_f32_e32 v24, 0xc1898193, v24
	v_exp_f32_e32 v27, v22
	v_exp_f32_e32 v28, v24
	v_fmamk_f32 v25, v151, 0xbc5083aa, v15
	v_add_f32_e32 v27, 1.0, v27
	v_rcp_f32_e32 v27, v27
	v_add_f32_e32 v28, 1.0, v28
	v_rcp_f32_e32 v28, v28
	v_med3_f32 v25, v25, s76, v225
	v_fmamk_f32 v26, v147, 0xbc5083aa, v3
	v_med3_f32 v26, v26, s76, v225
	v_mul_f32_e32 v22, v22, v27
	v_mul_f32_e32 v22, v25, v22
	v_mul_f32_e32 v24, v24, v28
	v_mul_f32_e32 v24, v26, v24
	v_fmamk_f32 v25, v160, 0xbd9d265f, v12
	v_max_f32_e32 v25, 0xc1898193, v25
	v_fmamk_f32 v26, v156, 0xbd9d265f, v8
	v_max_f32_e32 v26, 0xc1898193, v26
	v_exp_f32_e32 v29, v25
	v_exp_f32_e32 v30, v26
	v_fmamk_f32 v27, v152, 0xbc5083aa, v16
	v_add_f32_e32 v29, 1.0, v29
	v_rcp_f32_e32 v29, v29
	v_add_f32_e32 v30, 1.0, v30
	v_rcp_f32_e32 v30, v30
	v_med3_f32 v27, v27, s76, v225
	v_fmamk_f32 v28, v148, 0xbc5083aa, v4
	v_med3_f32 v28, v28, s76, v225
	v_mul_f32_e32 v25, v25, v29
	v_mul_f32_e32 v25, v27, v25
	v_mul_f32_e32 v26, v26, v30
	v_mul_f32_e32 v26, v28, v26
	v_fmamk_f32 v27, v161, 0xbd9d265f, v13
	v_max_f32_e32 v27, 0xc1898193, v27
	v_fmamk_f32 v28, v157, 0xbd9d265f, v9
	v_max_f32_e32 v28, 0xc1898193, v28
	v_exp_f32_e32 v31, v27
	v_exp_f32_e32 v32, v28
	v_fmamk_f32 v29, v153, 0xbc5083aa, v17
	v_add_f32_e32 v31, 1.0, v31
	v_rcp_f32_e32 v31, v31
	v_add_f32_e32 v32, 1.0, v32
	v_rcp_f32_e32 v32, v32
	v_med3_f32 v29, v29, s76, v225
	v_fmamk_f32 v30, v149, 0xbc5083aa, v5
	v_med3_f32 v30, v30, s76, v225
	v_mul_f32_e32 v27, v27, v31
	v_mul_f32_e32 v27, v29, v27
	v_mul_f32_e32 v28, v28, v32
	v_mul_f32_e32 v28, v30, v28
	v_mov_b32_e32 v29, v22
	v_mov_b32_e32 v22, v201
	v_cvt_pk_fp8_f32 v22, v21, v29
	v_mov_b32_e32 v21, v23
	v_mov_b32_e32 v23, v201
	v_cvt_pk_fp8_f32 v23, v21, v24
	v_cvt_pk_fp8_f32 v23, v26, v28 op_sel:[0, 0, 1]
	v_fmamk_f32 v21, v142, 0xbd9d265f, v10
	v_max_f32_e32 v21, 0xc1898193, v21
	v_fmamk_f32 v24, v138, 0xbd9d265f, v6
	v_cvt_pk_fp8_f32 v22, v25, v27 op_sel:[0,0,1]
	v_max_f32_e32 v24, 0xc1898193, v24
	v_exp_f32_e32 v27, v21
	v_exp_f32_e32 v28, v24
	v_fmamk_f32 v25, v134, 0xbc5083aa, v14
	v_add_f32_e32 v27, 1.0, v27
	v_rcp_f32_e32 v27, v27
	v_add_f32_e32 v28, 1.0, v28
	v_rcp_f32_e32 v28, v28
	v_med3_f32 v25, v25, s76, v225
	v_fmamk_f32 v26, v130, 0xbc5083aa, v2
	v_med3_f32 v26, v26, s76, v225
	v_mul_f32_e32 v21, v21, v27
	v_mul_f32_e32 v21, v25, v21
	v_mul_f32_e32 v24, v24, v28
	v_mov_b32_e32 v25, v26
	v_mul_f32_e32 v25, v25, v24
	v_fmamk_f32 v24, v143, 0xbd9d265f, v11
	v_max_f32_e32 v24, 0xc1898193, v24
	v_fmamk_f32 v26, v139, 0xbd9d265f, v7
	v_max_f32_e32 v26, 0xc1898193, v26
	v_exp_f32_e32 v29, v24
	v_exp_f32_e32 v30, v26
	v_fmamk_f32 v27, v135, 0xbc5083aa, v15
	v_add_f32_e32 v29, 1.0, v29
	v_rcp_f32_e32 v29, v29
	v_add_f32_e32 v30, 1.0, v30
	v_rcp_f32_e32 v30, v30
	v_med3_f32 v27, v27, s76, v225
	v_fmamk_f32 v28, v131, 0xbc5083aa, v3
	v_med3_f32 v28, v28, s76, v225
	v_mul_f32_e32 v24, v24, v29
	v_mul_f32_e32 v24, v27, v24
	v_mul_f32_e32 v26, v26, v30
	v_mul_f32_e32 v26, v28, v26
	v_fmamk_f32 v27, v144, 0xbd9d265f, v12
	v_max_f32_e32 v27, 0xc1898193, v27
	v_fmamk_f32 v28, v140, 0xbd9d265f, v8
	v_max_f32_e32 v28, 0xc1898193, v28
	v_exp_f32_e32 v31, v27
	v_exp_f32_e32 v32, v28
	v_fmamk_f32 v29, v136, 0xbc5083aa, v16
	v_add_f32_e32 v31, 1.0, v31
	v_rcp_f32_e32 v31, v31
	v_add_f32_e32 v32, 1.0, v32
	v_rcp_f32_e32 v32, v32
	v_med3_f32 v29, v29, s76, v225
	v_fmamk_f32 v30, v132, 0xbc5083aa, v4
	v_med3_f32 v30, v30, s76, v225
	v_mul_f32_e32 v27, v27, v31
	v_mul_f32_e32 v27, v29, v27
	v_mul_f32_e32 v28, v28, v32
	v_mul_f32_e32 v28, v30, v28
	v_fmamk_f32 v29, v145, 0xbd9d265f, v13
	v_max_f32_e32 v29, 0xc1898193, v29
	v_fmamk_f32 v30, v141, 0xbd9d265f, v9
	v_max_f32_e32 v30, 0xc1898193, v30
	v_exp_f32_e32 v33, v29
	v_exp_f32_e32 v34, v30
	v_fmamk_f32 v31, v137, 0xbc5083aa, v17
	v_add_f32_e32 v33, 1.0, v33
	v_rcp_f32_e32 v33, v33
	v_add_f32_e32 v34, 1.0, v34
	v_rcp_f32_e32 v34, v34
	v_med3_f32 v31, v31, s76, v225
	v_fmamk_f32 v32, v133, 0xbc5083aa, v5
	v_med3_f32 v32, v32, s76, v225
	v_mul_f32_e32 v29, v29, v33
	v_mul_f32_e32 v29, v31, v29
	v_mul_f32_e32 v30, v30, v34
	v_mul_f32_e32 v30, v32, v30
	v_mov_b32_e32 v31, v24
; __device__ __forceinline__ float sigmoidf_(float x) { return __builtin_amdgcn_rcpf(1.0f + __builtin_amdgcn_exp2f(-1.44269504089f * x)); }
;     __device__ __forceinline__ void operator()(EPI_ARGS) const {
;     ...
;                 for (int h = 0; h < 2; ++h) { const int m = 2 * mp + h;
;                     const f32x4 a0 = acc[ai][0][m][0] * 0.03125f + ba0, a1 = acc[ai][0][m][1] * 0.03125f + ba1, l0 = acc[ai][1][m][0] * 0.03125f + bl0, l1 = acc[ai][1][m][1] * 0.03125f + bl1;
;                     float o[8];
; #pragma unroll
;                     for (int j = 0; j < 4; ++j) { const float g0 = fminf(a0[j], 7.0f), g1 = fminf(a1[j], 7.0f), x0 = fminf(fmaxf(l0[j], -7.0f), 7.0f), x1 = fminf(fmaxf(l1[j], -7.0f), 7.0f);
;                         o[j] = g0 * sigmoidf_(1.702f * g0) * (x0 + 1.0f); o[4 + j] = g1 * sigmoidf_(1.702f * g1) * (x1 + 1.0f); }
;                     px[h] = pk4_fp8(o[0], o[1], o[2], o[3]); py[h] = pk4_fp8(o[4], o[5], o[6], o[7]); }
;                 const u32x4 q = pair16(px[0], py[0], px[1], py[1]);
;                 const int row = u.pm * 256 + ai * 128 + wr * 64 + (2 * mp + (fq & 1)) * 16 + fr;
;                 *(u32x4*)(ACT + (size_t)row * FE + j0q) = q; }
	v_mov_b32_e32 v24, v201
	v_cvt_pk_fp8_f32 v24, v21, v31
	v_mov_b32_e32 v21, v25
	v_mov_b32_e32 v25, v201
	v_cvt_pk_fp8_f32 v25, v21, v26
	v_cvt_pk_fp8_f32 v24, v27, v29 op_sel:[0,0,1]
	v_cvt_pk_fp8_f32 v25, v28, v30 op_sel:[0, 0, 1]
	v_add_u32_e32 v26, s8, v220
	v_ashrrev_i32_e32 v27, 31, v26
	v_lshlrev_b64 v[26:27], 11, v[26:27]
	v_lshl_add_u64 v[26:27], s[16:17], 0, v[26:27]
	v_permlane16_swap_b32_e32 v22, v24
	v_permlane16_swap_b32_e32 v23, v25
	v_lshl_add_u64 v[26:27], v[26:27], 0, v[18:19]
	v_fmamk_f32 v21, v126, 0xbd9d265f, v10
	global_store_dwordx4 v[26:27], v[22:25], off
	v_max_f32_e32 v21, 0xc1898193, v21
	s_nop 0
	v_fmamk_f32 v22, v122, 0xbd9d265f, v6
	v_max_f32_e32 v22, 0xc1898193, v22
	v_exp_f32_e32 v25, v21
	v_exp_f32_e32 v26, v22
	v_fmamk_f32 v23, v118, 0xbc5083aa, v14
	v_add_f32_e32 v25, 1.0, v25
	v_rcp_f32_e32 v25, v25
	v_add_f32_e32 v26, 1.0, v26
	v_rcp_f32_e32 v26, v26
	v_med3_f32 v23, v23, s76, v225
	v_fmamk_f32 v24, v114, 0xbc5083aa, v2
	v_med3_f32 v24, v24, s76, v225
	v_mul_f32_e32 v21, v21, v25
	v_mul_f32_e32 v21, v23, v21
	v_mul_f32_e32 v22, v22, v26
	v_mov_b32_e32 v23, v24
	v_mul_f32_e32 v23, v23, v22
	v_fmamk_f32 v22, v127, 0xbd9d265f, v11
	v_max_f32_e32 v22, 0xc1898193, v22
	v_fmamk_f32 v24, v123, 0xbd9d265f, v7
	v_max_f32_e32 v24, 0xc1898193, v24
	v_exp_f32_e32 v27, v22
	v_exp_f32_e32 v28, v24
	v_fmamk_f32 v25, v119, 0xbc5083aa, v15
	v_add_f32_e32 v27, 1.0, v27
	v_rcp_f32_e32 v27, v27
	v_add_f32_e32 v28, 1.0, v28
	v_rcp_f32_e32 v28, v28
	v_med3_f32 v25, v25, s76, v225
	v_fmamk_f32 v26, v115, 0xbc5083aa, v3
	v_med3_f32 v26, v26, s76, v225
	v_mul_f32_e32 v22, v22, v27
	v_mul_f32_e32 v22, v25, v22
	v_mul_f32_e32 v24, v24, v28
	v_mul_f32_e32 v24, v26, v24
	v_fmamk_f32 v25, v128, 0xbd9d265f, v12
	v_max_f32_e32 v25, 0xc1898193, v25
	v_fmamk_f32 v26, v124, 0xbd9d265f, v8
	v_max_f32_e32 v26, 0xc1898193, v26
	v_exp_f32_e32 v29, v25
	v_exp_f32_e32 v30, v26
	v_fmamk_f32 v27, v120, 0xbc5083aa, v16
	v_add_f32_e32 v29, 1.0, v29
	v_rcp_f32_e32 v29, v29
	v_add_f32_e32 v30, 1.0, v30
	v_rcp_f32_e32 v30, v30
	v_med3_f32 v27, v27, s76, v225
	v_fmamk_f32 v28, v116, 0xbc5083aa, v4
	v_med3_f32 v28, v28, s76, v225
	v_mul_f32_e32 v25, v25, v29
	v_mul_f32_e32 v25, v27, v25
	v_mul_f32_e32 v26, v26, v30
	v_mul_f32_e32 v26, v28, v26
	v_fmamk_f32 v27, v129, 0xbd9d265f, v13
	v_max_f32_e32 v27, 0xc1898193, v27
	v_fmamk_f32 v28, v125, 0xbd9d265f, v9
	v_max_f32_e32 v28, 0xc1898193, v28
	v_exp_f32_e32 v31, v27
	v_exp_f32_e32 v32, v28
	v_fmamk_f32 v29, v121, 0xbc5083aa, v17
	v_add_f32_e32 v31, 1.0, v31
	v_rcp_f32_e32 v31, v31
	v_add_f32_e32 v32, 1.0, v32
	v_rcp_f32_e32 v32, v32
	v_med3_f32 v29, v29, s76, v225
	v_fmamk_f32 v30, v117, 0xbc5083aa, v5
	v_med3_f32 v30, v30, s76, v225
	v_mul_f32_e32 v27, v27, v31
	v_mul_f32_e32 v27, v29, v27
	v_mul_f32_e32 v28, v28, v32
	v_mul_f32_e32 v28, v30, v28
	v_mov_b32_e32 v29, v22
	v_mov_b32_e32 v22, v201
	v_cvt_pk_fp8_f32 v22, v21, v29
	v_mov_b32_e32 v21, v23
	v_mov_b32_e32 v23, v201
	v_cvt_pk_fp8_f32 v23, v21, v24
	v_cvt_pk_fp8_f32 v23, v26, v28 op_sel:[0, 0, 1]
	v_fmamk_f32 v21, v110, 0xbd9d265f, v10
	v_max_f32_e32 v21, 0xc1898193, v21
	v_fmamk_f32 v24, v106, 0xbd9d265f, v6
	v_cvt_pk_fp8_f32 v22, v25, v27 op_sel:[0,0,1]
	v_max_f32_e32 v24, 0xc1898193, v24
	v_exp_f32_e32 v27, v21
	v_exp_f32_e32 v28, v24
	v_fmamk_f32 v25, v102, 0xbc5083aa, v14
	v_add_f32_e32 v27, 1.0, v27
	v_rcp_f32_e32 v27, v27
	v_add_f32_e32 v28, 1.0, v28
	v_rcp_f32_e32 v28, v28
	v_med3_f32 v25, v25, s76, v225
	v_fmamk_f32 v26, v98, 0xbc5083aa, v2
	v_med3_f32 v26, v26, s76, v225
	v_mul_f32_e32 v21, v21, v27
	v_mul_f32_e32 v21, v25, v21
	v_mul_f32_e32 v24, v24, v28
	v_mov_b32_e32 v25, v26
	v_mul_f32_e32 v25, v25, v24
	v_fmamk_f32 v24, v111, 0xbd9d265f, v11
	v_max_f32_e32 v24, 0xc1898193, v24
	v_fmamk_f32 v26, v107, 0xbd9d265f, v7
	v_max_f32_e32 v26, 0xc1898193, v26
	v_exp_f32_e32 v29, v24
	v_exp_f32_e32 v30, v26
	v_fmamk_f32 v27, v103, 0xbc5083aa, v15
	v_add_f32_e32 v29, 1.0, v29
	v_rcp_f32_e32 v29, v29
	v_add_f32_e32 v30, 1.0, v30
	v_rcp_f32_e32 v30, v30
	v_med3_f32 v27, v27, s76, v225
	v_fmamk_f32 v28, v99, 0xbc5083aa, v3
	v_med3_f32 v28, v28, s76, v225
	v_mul_f32_e32 v24, v24, v29
	v_mul_f32_e32 v24, v27, v24
	v_mul_f32_e32 v26, v26, v30
	v_mul_f32_e32 v26, v28, v26
	v_fmamk_f32 v27, v112, 0xbd9d265f, v12
	v_max_f32_e32 v27, 0xc1898193, v27
	v_fmamk_f32 v28, v108, 0xbd9d265f, v8
	v_max_f32_e32 v28, 0xc1898193, v28
	v_exp_f32_e32 v31, v27
	v_exp_f32_e32 v32, v28
	v_fmamk_f32 v29, v104, 0xbc5083aa, v16
	v_add_f32_e32 v31, 1.0, v31
	v_rcp_f32_e32 v31, v31
	v_add_f32_e32 v32, 1.0, v32
	v_rcp_f32_e32 v32, v32
	v_med3_f32 v29, v29, s76, v225
	v_fmamk_f32 v30, v100, 0xbc5083aa, v4
	v_med3_f32 v30, v30, s76, v225
	v_mul_f32_e32 v27, v27, v31
	v_mul_f32_e32 v27, v29, v27
	v_mul_f32_e32 v28, v28, v32
	v_mul_f32_e32 v28, v30, v28
	v_fmamk_f32 v29, v113, 0xbd9d265f, v13
	v_max_f32_e32 v29, 0xc1898193, v29
	v_fmamk_f32 v30, v109, 0xbd9d265f, v9
	v_max_f32_e32 v30, 0xc1898193, v30
	v_exp_f32_e32 v33, v29
	v_exp_f32_e32 v34, v30
	v_fmamk_f32 v31, v105, 0xbc5083aa, v17
	v_add_f32_e32 v33, 1.0, v33
	v_rcp_f32_e32 v33, v33
	v_add_f32_e32 v34, 1.0, v34
	v_rcp_f32_e32 v34, v34
	v_med3_f32 v31, v31, s76, v225
	v_fmamk_f32 v32, v101, 0xbc5083aa, v5
	v_med3_f32 v32, v32, s76, v225
	v_mul_f32_e32 v29, v29, v33
	v_mul_f32_e32 v29, v31, v29
	v_mul_f32_e32 v30, v30, v34
	v_mul_f32_e32 v30, v32, v30
	v_mov_b32_e32 v31, v24
	v_mov_b32_e32 v24, v201
	v_cvt_pk_fp8_f32 v24, v21, v31
	v_mov_b32_e32 v21, v25
	v_mov_b32_e32 v25, v201
	v_cvt_pk_fp8_f32 v25, v21, v26
	v_cvt_pk_fp8_f32 v24, v27, v29 op_sel:[0,0,1]
; __device__ __forceinline__ float sigmoidf_(float x) { return __builtin_amdgcn_rcpf(1.0f + __builtin_amdgcn_exp2f(-1.44269504089f * x)); }
;     __device__ __forceinline__ void operator()(EPI_ARGS) const {
;     ...
;                 for (int h = 0; h < 2; ++h) { const int m = 2 * mp + h;
;                     const f32x4 a0 = acc[ai][0][m][0] * 0.03125f + ba0, a1 = acc[ai][0][m][1] * 0.03125f + ba1, l0 = acc[ai][1][m][0] * 0.03125f + bl0, l1 = acc[ai][1][m][1] * 0.03125f + bl1;
;                     float o[8];
; #pragma unroll
;                     for (int j = 0; j < 4; ++j) { const float g0 = fminf(a0[j], 7.0f), g1 = fminf(a1[j], 7.0f), x0 = fminf(fmaxf(l0[j], -7.0f), 7.0f), x1 = fminf(fmaxf(l1[j], -7.0f), 7.0f);
;                         o[j] = g0 * sigmoidf_(1.702f * g0) * (x0 + 1.0f); o[4 + j] = g1 * sigmoidf_(1.702f * g1) * (x1 + 1.0f); }
;                     px[h] = pk4_fp8(o[0], o[1], o[2], o[3]); py[h] = pk4_fp8(o[4], o[5], o[6], o[7]); }
;                 const u32x4 q = pair16(px[0], py[0], px[1], py[1]);
;                 const int row = u.pm * 256 + ai * 128 + wr * 64 + (2 * mp + (fq & 1)) * 16 + fr;
;                 *(u32x4*)(ACT + (size_t)row * FE + j0q) = q; }
	v_cvt_pk_fp8_f32 v25, v28, v30 op_sel:[0, 0, 1]
	v_add_u32_e32 v26, 0x80, v20
	v_ashrrev_i32_e32 v27, 31, v26
	v_lshlrev_b64 v[26:27], 11, v[26:27]
	v_lshl_add_u64 v[26:27], s[16:17], 0, v[26:27]
	v_permlane16_swap_b32_e32 v22, v24
	v_permlane16_swap_b32_e32 v23, v25
	v_lshl_add_u64 v[26:27], v[26:27], 0, v[18:19]
	v_fmamk_f32 v21, v94, 0xbd9d265f, v10
	global_store_dwordx4 v[26:27], v[22:25], off
	v_max_f32_e32 v21, 0xc1898193, v21
	v_fmamk_f32 v10, v78, 0xbd9d265f, v10
	v_fmamk_f32 v22, v90, 0xbd9d265f, v6
	v_max_f32_e32 v22, 0xc1898193, v22
	v_exp_f32_e32 v25, v21
	v_exp_f32_e32 v26, v22
	v_fmamk_f32 v23, v86, 0xbc5083aa, v14
	v_add_f32_e32 v25, 1.0, v25
	v_rcp_f32_e32 v25, v25
	v_add_f32_e32 v26, 1.0, v26
	v_rcp_f32_e32 v26, v26
	v_med3_f32 v23, v23, s76, v225
	v_fmamk_f32 v24, v82, 0xbc5083aa, v2
	v_med3_f32 v24, v24, s76, v225
	v_mul_f32_e32 v21, v21, v25
	v_mul_f32_e32 v21, v23, v21
	v_mul_f32_e32 v22, v22, v26
	v_mov_b32_e32 v23, v24
	v_mul_f32_e32 v23, v23, v22
	v_fmamk_f32 v22, v95, 0xbd9d265f, v11
	v_max_f32_e32 v22, 0xc1898193, v22
	v_fmamk_f32 v24, v91, 0xbd9d265f, v7
	v_max_f32_e32 v24, 0xc1898193, v24
	v_exp_f32_e32 v27, v22
	v_exp_f32_e32 v28, v24
	v_fmamk_f32 v25, v87, 0xbc5083aa, v15
	v_add_f32_e32 v27, 1.0, v27
	v_rcp_f32_e32 v27, v27
	v_add_f32_e32 v28, 1.0, v28
	v_rcp_f32_e32 v28, v28
	v_med3_f32 v25, v25, s76, v225
	v_fmamk_f32 v26, v83, 0xbc5083aa, v3
	v_med3_f32 v26, v26, s76, v225
	v_mul_f32_e32 v22, v22, v27
	v_mul_f32_e32 v22, v25, v22
	v_mul_f32_e32 v24, v24, v28
	v_mul_f32_e32 v24, v26, v24
	v_fmamk_f32 v25, v96, 0xbd9d265f, v12
	v_max_f32_e32 v25, 0xc1898193, v25
	v_fmamk_f32 v26, v92, 0xbd9d265f, v8
	v_max_f32_e32 v26, 0xc1898193, v26
	v_exp_f32_e32 v29, v25
	v_exp_f32_e32 v30, v26
	v_fmamk_f32 v27, v88, 0xbc5083aa, v16
	v_add_f32_e32 v29, 1.0, v29
	v_rcp_f32_e32 v29, v29
	v_add_f32_e32 v30, 1.0, v30
	v_rcp_f32_e32 v30, v30
	v_med3_f32 v27, v27, s76, v225
	v_fmamk_f32 v28, v84, 0xbc5083aa, v4
	v_med3_f32 v28, v28, s76, v225
	v_mul_f32_e32 v25, v25, v29
	v_mul_f32_e32 v25, v27, v25
	v_mul_f32_e32 v26, v26, v30
	v_mul_f32_e32 v26, v28, v26
	v_fmamk_f32 v27, v97, 0xbd9d265f, v13
	v_max_f32_e32 v27, 0xc1898193, v27
	v_fmamk_f32 v28, v93, 0xbd9d265f, v9
	v_max_f32_e32 v28, 0xc1898193, v28
	v_exp_f32_e32 v31, v27
	v_exp_f32_e32 v32, v28
	v_fmamk_f32 v29, v89, 0xbc5083aa, v17
	v_add_f32_e32 v31, 1.0, v31
	v_rcp_f32_e32 v31, v31
	v_add_f32_e32 v32, 1.0, v32
	v_rcp_f32_e32 v32, v32
	v_med3_f32 v29, v29, s76, v225
	v_fmamk_f32 v30, v85, 0xbc5083aa, v5
	v_med3_f32 v30, v30, s76, v225
	v_mul_f32_e32 v27, v27, v31
	v_mul_f32_e32 v27, v29, v27
	v_mul_f32_e32 v28, v28, v32
	v_mul_f32_e32 v28, v30, v28
	v_mov_b32_e32 v29, v22
	v_mov_b32_e32 v22, v201
	v_cvt_pk_fp8_f32 v22, v21, v29
	v_mov_b32_e32 v21, v23
	v_mov_b32_e32 v23, v201
	v_cvt_pk_fp8_f32 v23, v21, v24
	v_fmamk_f32 v6, v74, 0xbd9d265f, v6
	v_max_f32_e32 v6, 0xc1898193, v6
	v_cvt_pk_fp8_f32 v23, v26, v28 op_sel:[0, 0, 1]
	v_max_f32_e32 v10, 0xc1898193, v10
	v_exp_f32_e32 v24, v6
	v_exp_f32_e32 v21, v10
	v_fmamk_f32 v2, v66, 0xbc5083aa, v2
	v_add_f32_e32 v24, 1.0, v24
	v_rcp_f32_e32 v24, v24
	v_add_f32_e32 v21, 1.0, v21
	v_rcp_f32_e32 v21, v21
	v_med3_f32 v2, v2, s76, v225
	v_fmamk_f32 v14, v70, 0xbc5083aa, v14
	v_mul_f32_e32 v6, v6, v24
	v_med3_f32 v14, v14, s76, v225
	v_mul_f32_e32 v2, v2, v6
	v_fmamk_f32 v6, v79, 0xbd9d265f, v11
	v_mul_f32_e32 v10, v10, v21
	v_max_f32_e32 v6, 0xc1898193, v6
	v_fmamk_f32 v7, v75, 0xbd9d265f, v7
	v_mul_f32_e32 v10, v14, v10
	v_max_f32_e32 v7, 0xc1898193, v7
	v_fmamk_f32 v11, v71, 0xbc5083aa, v15
	v_exp_f32_e32 v14, v6
	v_exp_f32_e32 v15, v7
	v_fmamk_f32 v8, v76, 0xbd9d265f, v8
	v_add_f32_e32 v14, 1.0, v14
	v_rcp_f32_e32 v14, v14
	v_add_f32_e32 v15, 1.0, v15
	v_rcp_f32_e32 v15, v15
	v_fmamk_f32 v3, v67, 0xbc5083aa, v3
	v_max_f32_e32 v8, 0xc1898193, v8
	v_med3_f32 v3, v3, s76, v225
	v_mul_f32_e32 v6, v6, v14
	v_mul_f32_e32 v7, v7, v15
	v_mul_f32_e32 v3, v3, v7
	v_fmamk_f32 v7, v80, 0xbd9d265f, v12
	v_exp_f32_e32 v14, v8
	v_max_f32_e32 v7, 0xc1898193, v7
	v_exp_f32_e32 v12, v7
	v_add_f32_e32 v14, 1.0, v14
	v_rcp_f32_e32 v14, v14
	v_fmamk_f32 v4, v68, 0xbc5083aa, v4
	v_add_f32_e32 v12, 1.0, v12
	v_med3_f32 v4, v4, s76, v225
	v_fmac_f32_e32 v9, 0xbd9d265f, v77
	v_rcp_f32_e32 v12, v12
	v_mul_f32_e32 v8, v8, v14
	v_fmac_f32_e32 v13, 0xbd9d265f, v81
	v_max_f32_e32 v9, 0xc1898193, v9
	v_mul_f32_e32 v4, v4, v8
	v_max_f32_e32 v8, 0xc1898193, v13
	v_exp_f32_e32 v13, v9
	v_mul_f32_e32 v7, v7, v12
	v_exp_f32_e32 v12, v8
	v_add_f32_e32 v13, 1.0, v13
	v_rcp_f32_e32 v13, v13
	v_med3_f32 v11, v11, s76, v225
	v_fmac_f32_e32 v5, 0xbc5083aa, v69
	v_add_f32_e32 v12, 1.0, v12
	v_mul_f32_e32 v6, v11, v6
	v_fmamk_f32 v11, v72, 0xbc5083aa, v16
	v_rcp_f32_e32 v12, v12
	v_med3_f32 v5, v5, s76, v225
	v_med3_f32 v11, v11, s76, v225
	v_mul_f32_e32 v9, v9, v13
	v_cvt_pk_fp8_f32 v22, v25, v27 op_sel:[0,0,1]
	v_fmac_f32_e32 v17, 0xbc5083aa, v73
	v_mul_f32_e32 v5, v5, v9
	v_mov_b32_e32 v24, v201
	v_mov_b32_e32 v25, v201
	v_mul_f32_e32 v7, v11, v7
	v_med3_f32 v11, v17, s76, v225
	v_cvt_pk_fp8_f32 v24, v10, v6
	v_cvt_pk_fp8_f32 v25, v2, v3
	v_mul_f32_e32 v8, v8, v12
	v_mul_f32_e32 v8, v11, v8
	v_cvt_pk_fp8_f32 v24, v7, v8 op_sel:[0,0,1]
	v_cvt_pk_fp8_f32 v25, v4, v5 op_sel:[0, 0, 1]
	v_add_u32_e32 v2, 0xa0, v20
	v_ashrrev_i32_e32 v3, 31, v2
	v_lshlrev_b64 v[2:3], 11, v[2:3]
	v_lshl_add_u64 v[2:3], s[16:17], 0, v[2:3]
	v_permlane16_swap_b32_e32 v22, v24
	v_permlane16_swap_b32_e32 v23, v25
	v_lshl_add_u64 v[2:3], v[2:3], 0, v[18:19]
	global_store_dwordx4 v[2:3], v[22:25], off
	s_cbranch_vccnz .LBB0_1302
	s_branch .LBB0_1301
